# expert weight conversion of layers 1-3 partly moved from the prologue into grid-barrier waits of early workgroups
# baseline (speedup 1.0000x reference)
.LBB0_133:
	s_add_i32 s46, s41, s33
	s_add_i32 s2, s46, 0xffff8ea0
	s_cmp_lt_i32 s2, 0
	s_cbranch_scc1 .Lp0_noskip
	s_cmp_lt_i32 s2, 0x2800
	s_cbranch_scc1 .Lp0_skip
	s_add_i32 s2, s2, 0xffff9750
	s_cmp_lt_i32 s2, 0
	s_cbranch_scc1 .Lp0_noskip
	s_cmp_lt_i32 s2, 0x2800
	s_cbranch_scc1 .Lp0_skip
	s_add_i32 s2, s2, 0xffff9750
	s_cmp_lt_i32 s2, 0
	s_cbranch_scc1 .Lp0_noskip
	s_cmp_lt_i32 s2, 0x2800
	s_cbranch_scc0 .Lp0_noskip
.Lp0_skip:
	s_add_i32 s46, s46, 0x2800

.Lcvt_site_3:
	s_mov_b32 s31, 3
	s_branch .Lcvt_post
.Lcvt_site_5:
	s_mov_b32 s31, 5
	s_branch .Lcvt_post
.Lcvt_site_9:
	s_mov_b32 s31, 9
	s_branch .Lcvt_post
.Lcvt_site_10:
	s_mov_b32 s31, 10
	s_branch .Lcvt_post
.Lcvt_post:
	s_mov_b64 exec, -1
	s_cmp_ge_u32 s62, 3
	s_cbranch_scc1 .Lcvt_ret
	v_lshrrev_b32_e32 v2, 6, v0
	v_and_b32_e32 v3, 63, v0
	s_nop 0
	v_readfirstlane_b32 s25, v2
	s_nop 3
	s_cmp_eq_u32 s31, 5
	s_cbranch_scc0 .Lcvt_s10
	s_sub_i32 s27, s80, 16
	s_cmp_lt_i32 s27, 0
	s_cbranch_scc1 .Lcvt_ret
	s_mov_b32 s26, 3
	s_movk_i32 s30, 0
	s_branch .Lcvt_go
.Lcvt_s10:
	s_cmp_eq_u32 s31, 10
	s_cbranch_scc0 .Lcvt_s9
	s_sub_i32 s27, s63, 112
	s_cmp_lt_i32 s27, 0
	s_cbranch_scc1 .Lcvt_ret
	s_mov_b32 s26, 4
	s_movk_i32 s30, 5040
	s_branch .Lcvt_go
.Lcvt_s9:
	s_cmp_eq_u32 s31, 9
	s_cbranch_scc0 .Lcvt_s3
	s_sub_i32 s27, s63, 208
	s_cmp_lt_i32 s27, 0
	s_cbranch_scc1 .Lcvt_ret
	s_mov_b32 s26, 3
	s_movk_i32 s30, 9072
	s_branch .Lcvt_go
.Lcvt_s3:
	s_cmp_eq_u32 s31, 3
	s_cbranch_scc0 .Lcvt_ret
	s_sub_i32 s27, s63, 208
	s_cmp_lt_i32 s27, 0
	s_cbranch_scc1 .Lcvt_ret
	s_mov_b32 s26, 1
	s_movk_i32 s30, 10080
	s_branch .Lcvt_go
.Lcvt_go:
	s_mul_i32 s27, s27, 7
	s_add_i32 s27, s27, s25
	s_add_i32 s27, s27, -1
	s_mul_i32 s27, s27, s26
	s_add_i32 s30, s30, s27
	v_lshrrev_b32_e32 v4, 3, v3
	v_and_b32_e32 v5, 7, v3
	v_mul_u32_u24_e32 v7, 17, v4
	v_and_b32_e32 v8, 3, v3
	v_lshl_add_u32 v7, v8, 2, v7
	v_lshlrev_b32_e32 v7, 2, v7
	v_mul_u32_u24_e32 v8, 0x110, v5
	v_add_lshl_u32 v8, v8, v4, 2
	s_mul_i32 s17, s25, 0x2200
	v_add_u32_e32 v7, s17, v7
	v_add_u32_e32 v8, s17, v8
	v_lshlrev_b32_e32 v9, 10, v4
	v_lshl_add_u32 v9, v5, 4, v9
	v_add_u32_e32 v10, 0x2000, v9
.Lcvt_item:
	s_cmpk_ge_u32 s30, 10240
	s_cbranch_scc1 .Lcvt_ret
	s_add_i32 s6, s62, 1
	s_mov_b32 s5, s30
	s_lshr_b32 s7, s5, 8
	s_mul_i32 s7, s7, 0xaaab
	s_lshr_b32 s7, s7, 17
	s_mul_i32 s8, s7, 0x300
	s_sub_i32 s8, s5, s8
	s_lshl_b32 s9, s6, 5
	s_add_i32 s9, s9, s7
	s_load_dwordx2 s[2:3], s[0:1], 0x100
	s_mov_b32 s18, s9
	s_mov_b32 s19, 0
	s_cmp_lt_u32 s8, 0x200
	s_cbranch_scc0 .Lcvt_dn
	s_load_dwordx2 s[10:11], s[0:1], 0xd8
	s_lshr_b32 s12, s8, 6
	s_and_b32 s13, s8, 63
	s_lshr_b32 s14, s13, 2
	s_and_b32 s14, s14, 7
	s_lshl_b32 s14, s14, 3
	s_and_b32 s15, s13, 3
	s_add_i32 s14, s14, s15
	s_lshr_b32 s15, s13, 5
	s_lshl_b32 s15, s15, 2
	s_add_i32 s14, s14, s15
	s_mov_b32 s16, 13
	s_lshl_b64 s[20:21], s[18:19], 23
	s_lshl_b64 s[22:23], s[18:19], 21
	s_mov_b32 s24, 0x6000000
	s_branch .Lcvt_common
.Lcvt_dn:
	s_load_dwordx2 s[10:11], s[0:1], 0xe8
	s_add_i32 s8, s8, 0xfffffe00
	s_lshr_b32 s12, s8, 5
	s_and_b32 s13, s8, 31
	s_mov_b32 s14, s13
	s_mov_b32 s16, 12
	s_lshl_b64 s[20:21], s[18:19], 22
	s_lshl_b64 s[22:23], s[18:19], 20
	s_mov_b32 s24, 0x26000000
.Lcvt_common:
	v_lshlrev_b32_e32 v6, s16, v4
	v_lshl_add_u32 v6, v5, 4, v6
	s_waitcnt lgkmcnt(0)
	s_add_u32 s10, s10, s20
	s_addc_u32 s11, s11, s21
	s_add_i32 s17, s16, 7
	s_lshl_b32 s17, s12, s17
	s_add_u32 s10, s10, s17
	s_addc_u32 s11, s11, 0
	s_lshl_b32 s17, s13, 7
	s_add_u32 s10, s10, s17
	s_addc_u32 s11, s11, 0
	s_add_i32 s17, s16, 3
	s_lshl_b32 s17, 1, s17
	global_load_dwordx4 v[16:19], v6, s[10:11] nt
	s_add_u32 s10, s10, s17
	s_addc_u32 s11, s11, 0
	global_load_dwordx4 v[20:23], v6, s[10:11] nt
	s_add_u32 s10, s10, s17
	s_addc_u32 s11, s11, 0
	global_load_dwordx4 v[24:27], v6, s[10:11] nt
	s_add_u32 s10, s10, s17
	s_addc_u32 s11, s11, 0
	global_load_dwordx4 v[28:31], v6, s[10:11] nt
	s_add_u32 s10, s10, s17
	s_addc_u32 s11, s11, 0
	global_load_dwordx4 v[32:35], v6, s[10:11] nt
	s_add_u32 s10, s10, s17
	s_addc_u32 s11, s11, 0
	global_load_dwordx4 v[36:39], v6, s[10:11] nt
	s_add_u32 s10, s10, s17
	s_addc_u32 s11, s11, 0
	global_load_dwordx4 v[40:43], v6, s[10:11] nt
	s_add_u32 s10, s10, s17
	s_addc_u32 s11, s11, 0
	global_load_dwordx4 v[44:47], v6, s[10:11] nt
	s_add_u32 s10, s10, s17
	s_addc_u32 s11, s11, 0
	global_load_dwordx4 v[48:51], v6, s[10:11] nt
	s_add_u32 s10, s10, s17
	s_addc_u32 s11, s11, 0
	global_load_dwordx4 v[52:55], v6, s[10:11] nt
	s_add_u32 s10, s10, s17
	s_addc_u32 s11, s11, 0
	global_load_dwordx4 v[56:59], v6, s[10:11] nt
	s_add_u32 s10, s10, s17
	s_addc_u32 s11, s11, 0
	global_load_dwordx4 v[60:63], v6, s[10:11] nt
	s_add_u32 s10, s10, s17
	s_addc_u32 s11, s11, 0
	global_load_dwordx4 v[64:67], v6, s[10:11] nt
	s_add_u32 s10, s10, s17
	s_addc_u32 s11, s11, 0
	global_load_dwordx4 v[68:71], v6, s[10:11] nt
	s_add_u32 s10, s10, s17
	s_addc_u32 s11, s11, 0
	global_load_dwordx4 v[72:75], v6, s[10:11] nt
	s_add_u32 s10, s10, s17
	s_addc_u32 s11, s11, 0
	global_load_dwordx4 v[76:79], v6, s[10:11] nt
	s_add_u32 s22, s22, s2
	s_addc_u32 s23, s23, s3
	s_add_u32 s22, s22, s24
	s_addc_u32 s23, s23, 0
	s_lshl_b32 s17, s14, 15
	s_add_u32 s22, s22, s17
	s_addc_u32 s23, s23, 0
	s_lshl_b32 s17, s12, 7
	s_add_u32 s22, s22, s17
	s_addc_u32 s23, s23, 0
	s_mov_b32 s28, 0x0f0f0f0f
	s_mov_b32 s29, 0x0f0f0f0f
	s_waitcnt vmcnt(0)
	s_mov_b64 exec, s[28:29]
	v_mul_f32_e32 v80, 0x42000000, v16
	v_mul_f32_e32 v81, 0x42000000, v17
	v_mul_f32_e32 v82, 0x42000000, v18
	v_mul_f32_e32 v83, 0x42000000, v19
	ds_write_b32 v7, v80 offset:0
	ds_write_b32 v7, v81 offset:4
	ds_write_b32 v7, v82 offset:8
	ds_write_b32 v7, v83 offset:12
	v_mul_f32_e32 v80, 0x42000000, v20
	v_mul_f32_e32 v81, 0x42000000, v21
	v_mul_f32_e32 v82, 0x42000000, v22
	v_mul_f32_e32 v83, 0x42000000, v23
	ds_write_b32 v7, v80 offset:544
	ds_write_b32 v7, v81 offset:548
	ds_write_b32 v7, v82 offset:552
	ds_write_b32 v7, v83 offset:556
	v_mul_f32_e32 v80, 0x42000000, v24
	v_mul_f32_e32 v81, 0x42000000, v25
	v_mul_f32_e32 v82, 0x42000000, v26
	v_mul_f32_e32 v83, 0x42000000, v27
	ds_write_b32 v7, v80 offset:1088
	ds_write_b32 v7, v81 offset:1092
	ds_write_b32 v7, v82 offset:1096
	ds_write_b32 v7, v83 offset:1100
	v_mul_f32_e32 v80, 0x42000000, v28
	v_mul_f32_e32 v81, 0x42000000, v29
	v_mul_f32_e32 v82, 0x42000000, v30
	v_mul_f32_e32 v83, 0x42000000, v31
	ds_write_b32 v7, v80 offset:1632
	ds_write_b32 v7, v81 offset:1636
	ds_write_b32 v7, v82 offset:1640
	ds_write_b32 v7, v83 offset:1644
	v_mul_f32_e32 v80, 0x42000000, v32
	v_mul_f32_e32 v81, 0x42000000, v33
	v_mul_f32_e32 v82, 0x42000000, v34
	v_mul_f32_e32 v83, 0x42000000, v35
	ds_write_b32 v7, v80 offset:2176
	ds_write_b32 v7, v81 offset:2180
	ds_write_b32 v7, v82 offset:2184
	ds_write_b32 v7, v83 offset:2188
	v_mul_f32_e32 v80, 0x42000000, v36
	v_mul_f32_e32 v81, 0x42000000, v37
	v_mul_f32_e32 v82, 0x42000000, v38
	v_mul_f32_e32 v83, 0x42000000, v39
	ds_write_b32 v7, v80 offset:2720
	ds_write_b32 v7, v81 offset:2724
	ds_write_b32 v7, v82 offset:2728
	ds_write_b32 v7, v83 offset:2732
	v_mul_f32_e32 v80, 0x42000000, v40
	v_mul_f32_e32 v81, 0x42000000, v41
	v_mul_f32_e32 v82, 0x42000000, v42
	v_mul_f32_e32 v83, 0x42000000, v43
	ds_write_b32 v7, v80 offset:3264
	ds_write_b32 v7, v81 offset:3268
	ds_write_b32 v7, v82 offset:3272
	ds_write_b32 v7, v83 offset:3276
	v_mul_f32_e32 v80, 0x42000000, v44
	v_mul_f32_e32 v81, 0x42000000, v45
	v_mul_f32_e32 v82, 0x42000000, v46
	v_mul_f32_e32 v83, 0x42000000, v47
	ds_write_b32 v7, v80 offset:3808
	ds_write_b32 v7, v81 offset:3812
	ds_write_b32 v7, v82 offset:3816
	ds_write_b32 v7, v83 offset:3820
	v_mul_f32_e32 v80, 0x42000000, v48
	v_mul_f32_e32 v81, 0x42000000, v49
	v_mul_f32_e32 v82, 0x42000000, v50
	v_mul_f32_e32 v83, 0x42000000, v51
	ds_write_b32 v7, v80 offset:4352
	ds_write_b32 v7, v81 offset:4356
	ds_write_b32 v7, v82 offset:4360
	ds_write_b32 v7, v83 offset:4364
	v_mul_f32_e32 v80, 0x42000000, v52
	v_mul_f32_e32 v81, 0x42000000, v53
	v_mul_f32_e32 v82, 0x42000000, v54
	v_mul_f32_e32 v83, 0x42000000, v55
	ds_write_b32 v7, v80 offset:4896
	ds_write_b32 v7, v81 offset:4900
	ds_write_b32 v7, v82 offset:4904
	ds_write_b32 v7, v83 offset:4908
	v_mul_f32_e32 v80, 0x42000000, v56
	v_mul_f32_e32 v81, 0x42000000, v57
	v_mul_f32_e32 v82, 0x42000000, v58
	v_mul_f32_e32 v83, 0x42000000, v59
	ds_write_b32 v7, v80 offset:5440
	ds_write_b32 v7, v81 offset:5444
	ds_write_b32 v7, v82 offset:5448
	ds_write_b32 v7, v83 offset:5452
	v_mul_f32_e32 v80, 0x42000000, v60
	v_mul_f32_e32 v81, 0x42000000, v61
	v_mul_f32_e32 v82, 0x42000000, v62
	v_mul_f32_e32 v83, 0x42000000, v63
	ds_write_b32 v7, v80 offset:5984
	ds_write_b32 v7, v81 offset:5988
	ds_write_b32 v7, v82 offset:5992
	ds_write_b32 v7, v83 offset:5996
	v_mul_f32_e32 v80, 0x42000000, v64
	v_mul_f32_e32 v81, 0x42000000, v65
	v_mul_f32_e32 v82, 0x42000000, v66
	v_mul_f32_e32 v83, 0x42000000, v67
	ds_write_b32 v7, v80 offset:6528
	ds_write_b32 v7, v81 offset:6532
	ds_write_b32 v7, v82 offset:6536
	ds_write_b32 v7, v83 offset:6540
	v_mul_f32_e32 v80, 0x42000000, v68
	v_mul_f32_e32 v81, 0x42000000, v69
	v_mul_f32_e32 v82, 0x42000000, v70
	v_mul_f32_e32 v83, 0x42000000, v71
	ds_write_b32 v7, v80 offset:7072
	ds_write_b32 v7, v81 offset:7076
	ds_write_b32 v7, v82 offset:7080
	ds_write_b32 v7, v83 offset:7084
	v_mul_f32_e32 v80, 0x42000000, v72
	v_mul_f32_e32 v81, 0x42000000, v73
	v_mul_f32_e32 v82, 0x42000000, v74
	v_mul_f32_e32 v83, 0x42000000, v75
	ds_write_b32 v7, v80 offset:7616
	ds_write_b32 v7, v81 offset:7620
	ds_write_b32 v7, v82 offset:7624
	ds_write_b32 v7, v83 offset:7628
	v_mul_f32_e32 v80, 0x42000000, v76
	v_mul_f32_e32 v81, 0x42000000, v77
	v_mul_f32_e32 v82, 0x42000000, v78
	v_mul_f32_e32 v83, 0x42000000, v79
	ds_write_b32 v7, v80 offset:8160
	ds_write_b32 v7, v81 offset:8164
	ds_write_b32 v7, v82 offset:8168
	ds_write_b32 v7, v83 offset:8172
	s_mov_b64 exec, -1
	s_waitcnt lgkmcnt(0)
	ds_read_b32 v84, v8 offset:0
	ds_read_b32 v85, v8 offset:68
	ds_read_b32 v86, v8 offset:136
	ds_read_b32 v87, v8 offset:204
	ds_read_b32 v88, v8 offset:272
	ds_read_b32 v89, v8 offset:340
	ds_read_b32 v90, v8 offset:408
	ds_read_b32 v91, v8 offset:476
	ds_read_b32 v92, v8 offset:544
	ds_read_b32 v93, v8 offset:612
	ds_read_b32 v94, v8 offset:680
	ds_read_b32 v95, v8 offset:748
	ds_read_b32 v96, v8 offset:816
	ds_read_b32 v97, v8 offset:884
	ds_read_b32 v98, v8 offset:952
	ds_read_b32 v99, v8 offset:1020
	s_waitcnt lgkmcnt(0)
	v_cvt_pk_fp8_f32 v100, v84, v85
	s_nop 0
	v_cvt_pk_fp8_f32 v100, v86, v87 op_sel:[0,0,1]
	v_cvt_pk_fp8_f32 v101, v88, v89
	s_nop 0
	v_cvt_pk_fp8_f32 v101, v90, v91 op_sel:[0,0,1]
	v_cvt_pk_fp8_f32 v102, v92, v93
	s_nop 0
	v_cvt_pk_fp8_f32 v102, v94, v95 op_sel:[0,0,1]
	v_cvt_pk_fp8_f32 v103, v96, v97
	s_nop 0
	v_cvt_pk_fp8_f32 v103, v98, v99 op_sel:[0,0,1]
	s_nop 0
	global_store_dwordx4 v9, v[100:103], s[22:23]
	s_nop 1
	ds_read_b32 v84, v8 offset:32
	ds_read_b32 v85, v8 offset:100
	ds_read_b32 v86, v8 offset:168
	ds_read_b32 v87, v8 offset:236
	ds_read_b32 v88, v8 offset:304
	ds_read_b32 v89, v8 offset:372
	ds_read_b32 v90, v8 offset:440
	ds_read_b32 v91, v8 offset:508
	ds_read_b32 v92, v8 offset:576
	ds_read_b32 v93, v8 offset:644
	ds_read_b32 v94, v8 offset:712
	ds_read_b32 v95, v8 offset:780
	ds_read_b32 v96, v8 offset:848
	ds_read_b32 v97, v8 offset:916
	ds_read_b32 v98, v8 offset:984
	ds_read_b32 v99, v8 offset:1052
	s_waitcnt lgkmcnt(0)
	v_cvt_pk_fp8_f32 v100, v84, v85
	s_nop 0
	v_cvt_pk_fp8_f32 v100, v86, v87 op_sel:[0,0,1]
	v_cvt_pk_fp8_f32 v101, v88, v89
	s_nop 0
	v_cvt_pk_fp8_f32 v101, v90, v91 op_sel:[0,0,1]
	v_cvt_pk_fp8_f32 v102, v92, v93
	s_nop 0
	v_cvt_pk_fp8_f32 v102, v94, v95 op_sel:[0,0,1]
	v_cvt_pk_fp8_f32 v103, v96, v97
	s_nop 0
	v_cvt_pk_fp8_f32 v103, v98, v99 op_sel:[0,0,1]
	s_nop 0
	global_store_dwordx4 v10, v[100:103], s[22:23]
	s_nop 1
	s_waitcnt lgkmcnt(0)
	s_not_b64 s[28:29], s[28:29]
	s_add_u32 s22, s22, 0x4000
	s_addc_u32 s23, s23, 0
	s_mov_b64 exec, s[28:29]
	v_mul_f32_e32 v80, 0x42000000, v16
	v_mul_f32_e32 v81, 0x42000000, v17
	v_mul_f32_e32 v82, 0x42000000, v18
	v_mul_f32_e32 v83, 0x42000000, v19
	ds_write_b32 v7, v80 offset:0
	ds_write_b32 v7, v81 offset:4
	ds_write_b32 v7, v82 offset:8
	ds_write_b32 v7, v83 offset:12
	v_mul_f32_e32 v80, 0x42000000, v20
	v_mul_f32_e32 v81, 0x42000000, v21
	v_mul_f32_e32 v82, 0x42000000, v22
	v_mul_f32_e32 v83, 0x42000000, v23
	ds_write_b32 v7, v80 offset:544
	ds_write_b32 v7, v81 offset:548
	ds_write_b32 v7, v82 offset:552
	ds_write_b32 v7, v83 offset:556
	v_mul_f32_e32 v80, 0x42000000, v24
	v_mul_f32_e32 v81, 0x42000000, v25
	v_mul_f32_e32 v82, 0x42000000, v26
	v_mul_f32_e32 v83, 0x42000000, v27
	ds_write_b32 v7, v80 offset:1088
	ds_write_b32 v7, v81 offset:1092
	ds_write_b32 v7, v82 offset:1096
	ds_write_b32 v7, v83 offset:1100
	v_mul_f32_e32 v80, 0x42000000, v28
	v_mul_f32_e32 v81, 0x42000000, v29
	v_mul_f32_e32 v82, 0x42000000, v30
	v_mul_f32_e32 v83, 0x42000000, v31
	ds_write_b32 v7, v80 offset:1632
	ds_write_b32 v7, v81 offset:1636
	ds_write_b32 v7, v82 offset:1640
	ds_write_b32 v7, v83 offset:1644
	v_mul_f32_e32 v80, 0x42000000, v32
	v_mul_f32_e32 v81, 0x42000000, v33
	v_mul_f32_e32 v82, 0x42000000, v34
	v_mul_f32_e32 v83, 0x42000000, v35
	ds_write_b32 v7, v80 offset:2176
	ds_write_b32 v7, v81 offset:2180
	ds_write_b32 v7, v82 offset:2184
	ds_write_b32 v7, v83 offset:2188
	v_mul_f32_e32 v80, 0x42000000, v36
	v_mul_f32_e32 v81, 0x42000000, v37
	v_mul_f32_e32 v82, 0x42000000, v38
	v_mul_f32_e32 v83, 0x42000000, v39
	ds_write_b32 v7, v80 offset:2720
	ds_write_b32 v7, v81 offset:2724
	ds_write_b32 v7, v82 offset:2728
	ds_write_b32 v7, v83 offset:2732
	v_mul_f32_e32 v80, 0x42000000, v40
	v_mul_f32_e32 v81, 0x42000000, v41
	v_mul_f32_e32 v82, 0x42000000, v42
	v_mul_f32_e32 v83, 0x42000000, v43
	ds_write_b32 v7, v80 offset:3264
	ds_write_b32 v7, v81 offset:3268
	ds_write_b32 v7, v82 offset:3272
	ds_write_b32 v7, v83 offset:3276
	v_mul_f32_e32 v80, 0x42000000, v44
	v_mul_f32_e32 v81, 0x42000000, v45
	v_mul_f32_e32 v82, 0x42000000, v46
	v_mul_f32_e32 v83, 0x42000000, v47
	ds_write_b32 v7, v80 offset:3808
	ds_write_b32 v7, v81 offset:3812
	ds_write_b32 v7, v82 offset:3816
	ds_write_b32 v7, v83 offset:3820
	v_mul_f32_e32 v80, 0x42000000, v48
	v_mul_f32_e32 v81, 0x42000000, v49
	v_mul_f32_e32 v82, 0x42000000, v50
	v_mul_f32_e32 v83, 0x42000000, v51
	ds_write_b32 v7, v80 offset:4352
	ds_write_b32 v7, v81 offset:4356
	ds_write_b32 v7, v82 offset:4360
	ds_write_b32 v7, v83 offset:4364
	v_mul_f32_e32 v80, 0x42000000, v52
	v_mul_f32_e32 v81, 0x42000000, v53
	v_mul_f32_e32 v82, 0x42000000, v54
	v_mul_f32_e32 v83, 0x42000000, v55
	ds_write_b32 v7, v80 offset:4896
	ds_write_b32 v7, v81 offset:4900
	ds_write_b32 v7, v82 offset:4904
	ds_write_b32 v7, v83 offset:4908
	v_mul_f32_e32 v80, 0x42000000, v56
	v_mul_f32_e32 v81, 0x42000000, v57
	v_mul_f32_e32 v82, 0x42000000, v58
	v_mul_f32_e32 v83, 0x42000000, v59
	ds_write_b32 v7, v80 offset:5440
	ds_write_b32 v7, v81 offset:5444
	ds_write_b32 v7, v82 offset:5448
	ds_write_b32 v7, v83 offset:5452
	v_mul_f32_e32 v80, 0x42000000, v60
	v_mul_f32_e32 v81, 0x42000000, v61
	v_mul_f32_e32 v82, 0x42000000, v62
	v_mul_f32_e32 v83, 0x42000000, v63
	ds_write_b32 v7, v80 offset:5984
	ds_write_b32 v7, v81 offset:5988
	ds_write_b32 v7, v82 offset:5992
	ds_write_b32 v7, v83 offset:5996
	v_mul_f32_e32 v80, 0x42000000, v64
	v_mul_f32_e32 v81, 0x42000000, v65
	v_mul_f32_e32 v82, 0x42000000, v66
	v_mul_f32_e32 v83, 0x42000000, v67
	ds_write_b32 v7, v80 offset:6528
	ds_write_b32 v7, v81 offset:6532
	ds_write_b32 v7, v82 offset:6536
	ds_write_b32 v7, v83 offset:6540
	v_mul_f32_e32 v80, 0x42000000, v68
	v_mul_f32_e32 v81, 0x42000000, v69
	v_mul_f32_e32 v82, 0x42000000, v70
	v_mul_f32_e32 v83, 0x42000000, v71
	ds_write_b32 v7, v80 offset:7072
	ds_write_b32 v7, v81 offset:7076
	ds_write_b32 v7, v82 offset:7080
	ds_write_b32 v7, v83 offset:7084
	v_mul_f32_e32 v80, 0x42000000, v72
	v_mul_f32_e32 v81, 0x42000000, v73
	v_mul_f32_e32 v82, 0x42000000, v74
	v_mul_f32_e32 v83, 0x42000000, v75
	ds_write_b32 v7, v80 offset:7616
	ds_write_b32 v7, v81 offset:7620
	ds_write_b32 v7, v82 offset:7624
	ds_write_b32 v7, v83 offset:7628
	v_mul_f32_e32 v80, 0x42000000, v76
	v_mul_f32_e32 v81, 0x42000000, v77
	v_mul_f32_e32 v82, 0x42000000, v78
	v_mul_f32_e32 v83, 0x42000000, v79
	ds_write_b32 v7, v80 offset:8160
	ds_write_b32 v7, v81 offset:8164
	ds_write_b32 v7, v82 offset:8168
	ds_write_b32 v7, v83 offset:8172
	s_mov_b64 exec, -1
	s_waitcnt lgkmcnt(0)
	ds_read_b32 v84, v8 offset:0
	ds_read_b32 v85, v8 offset:68
	ds_read_b32 v86, v8 offset:136
	ds_read_b32 v87, v8 offset:204
	ds_read_b32 v88, v8 offset:272
	ds_read_b32 v89, v8 offset:340
	ds_read_b32 v90, v8 offset:408
	ds_read_b32 v91, v8 offset:476
	ds_read_b32 v92, v8 offset:544
	ds_read_b32 v93, v8 offset:612
	ds_read_b32 v94, v8 offset:680
	ds_read_b32 v95, v8 offset:748
	ds_read_b32 v96, v8 offset:816
	ds_read_b32 v97, v8 offset:884
	ds_read_b32 v98, v8 offset:952
	ds_read_b32 v99, v8 offset:1020
	s_waitcnt lgkmcnt(0)
	v_cvt_pk_fp8_f32 v100, v84, v85
	s_nop 0
	v_cvt_pk_fp8_f32 v100, v86, v87 op_sel:[0,0,1]
	v_cvt_pk_fp8_f32 v101, v88, v89
	s_nop 0
	v_cvt_pk_fp8_f32 v101, v90, v91 op_sel:[0,0,1]
	v_cvt_pk_fp8_f32 v102, v92, v93
	s_nop 0
	v_cvt_pk_fp8_f32 v102, v94, v95 op_sel:[0,0,1]
	v_cvt_pk_fp8_f32 v103, v96, v97
	s_nop 0
	v_cvt_pk_fp8_f32 v103, v98, v99 op_sel:[0,0,1]
	s_nop 0
	global_store_dwordx4 v9, v[100:103], s[22:23]
	s_nop 1
	ds_read_b32 v84, v8 offset:32
	ds_read_b32 v85, v8 offset:100
	ds_read_b32 v86, v8 offset:168
	ds_read_b32 v87, v8 offset:236
	ds_read_b32 v88, v8 offset:304
	ds_read_b32 v89, v8 offset:372
	ds_read_b32 v90, v8 offset:440
	ds_read_b32 v91, v8 offset:508
	ds_read_b32 v92, v8 offset:576
	ds_read_b32 v93, v8 offset:644
	ds_read_b32 v94, v8 offset:712
	ds_read_b32 v95, v8 offset:780
	ds_read_b32 v96, v8 offset:848
	ds_read_b32 v97, v8 offset:916
	ds_read_b32 v98, v8 offset:984
	ds_read_b32 v99, v8 offset:1052
	s_waitcnt lgkmcnt(0)
	v_cvt_pk_fp8_f32 v100, v84, v85
	s_nop 0
	v_cvt_pk_fp8_f32 v100, v86, v87 op_sel:[0,0,1]
	v_cvt_pk_fp8_f32 v101, v88, v89
	s_nop 0
	v_cvt_pk_fp8_f32 v101, v90, v91 op_sel:[0,0,1]
	v_cvt_pk_fp8_f32 v102, v92, v93
	s_nop 0
	v_cvt_pk_fp8_f32 v102, v94, v95 op_sel:[0,0,1]
	v_cvt_pk_fp8_f32 v103, v96, v97
	s_nop 0
	v_cvt_pk_fp8_f32 v103, v98, v99 op_sel:[0,0,1]
	s_nop 0
	global_store_dwordx4 v10, v[100:103], s[22:23]
	s_nop 1
	s_add_i32 s30, s30, 1
	s_add_i32 s26, s26, -1
	s_cmp_lg_u32 s26, 0
	s_cbranch_scc1 .Lcvt_item
.Lcvt_ret:
	s_mov_b64 exec, -1
	s_cmp_eq_u32 s31, 0
	s_cbranch_scc1 .LBB0_326
	s_cmp_eq_u32 s31, 1
	s_cbranch_scc1 .LBB0_404
	s_cmp_eq_u32 s31, 2
	s_cbranch_scc1 .LBB0_533
	s_cmp_eq_u32 s31, 3
	s_cbranch_scc1 .LBB0_610
	s_cmp_eq_u32 s31, 4
	s_cbranch_scc1 .LBB0_673
	s_cmp_eq_u32 s31, 5
	s_cbranch_scc1 .LBB0_849
	s_cmp_eq_u32 s31, 6
	s_cbranch_scc1 .LBB0_955
	s_cmp_eq_u32 s31, 7
	s_cbranch_scc1 .LBB0_1074
	s_cmp_eq_u32 s31, 8
	s_cbranch_scc1 .LBB0_1171
	s_cmp_eq_u32 s31, 9
	s_cbranch_scc1 .LBB0_1342
	s_cmp_eq_u32 s31, 10
	s_cbranch_scc1 .LBB0_245
	s_branch .LBB0_326
